# diff attention: per-XCD work queues (units of a (b,h) pair stay on one XCD for L2 reuse of its K/V stream)
# speedup vs baseline: 1.0080x; 1.0044x over previous
; #define LAS __attribute__((address_space(3)))
; __device__ __forceinline__ int lt_tid(int wv) { int ln; asm volatile("v_mbcnt_lo_u32_b32 %0, -1, 0\n\tv_mbcnt_hi_u32_b32 %0, -1, %0" : "=v"(ln)); return (wv << 6) | ln; }
;     ...
;     const int tid = lt_tid(wvid), lane = tid & 63, wave = __builtin_amdgcn_readfirstlane(tid >> 6), l31 = lane & 31, hi = lane >> 5;
;     const bf16_t* U = (const bf16_t*)(ws + WS_U); const bf16_t* VT = (const bf16_t*)(ws + WS_VTD); bf16_t* MIX = (bf16_t*)(ws + WS_MIX);
;     unsigned* qhead = (unsigned*)(ws + WS_CTL) + CW_DQ + (qslot * 4 + l) * 64;
;     LAS float* btab = (LAS float*)lds;
;     LAS int* ucur = (LAS int*)(lds + 4 * 132 * 4);
;     LAS unsigned char* KV = lds + 4096;
;     constexpr float LOG2E = 1.4426950408889634f;
;     for (int i = tid; i < 4 * 129; i += NTHR) { const int h = i / 129, n = i % 129; btab[h * 132 + n] = p.in[I_RELB][t5_bucket(n) * 8 + 4 + h] * 5.656854249492381f; }
.LBB0_760:
	s_getreg_b32 s64, hwreg(HW_REG_XCC_ID, 0, 4)
	s_and_b32 s64, s64, 7
	s_mov_b32 s0, s65
	s_mov_b64 s[6:7], s[66:67]
	s_waitcnt vmcnt(1)
	v_mbcnt_lo_u32_b32 v32, -1, 0
	v_mbcnt_hi_u32_b32 v32, -1, v32
	s_movk_i32 s0, 0x204
	v_or_b32_e32 v30, s75, v32
	v_cmp_gt_i32_e32 vcc, s0, v30
	v_readfirstlane_b32 s20, v30
	s_and_saveexec_b64 s[0:1], vcc
	s_cbranch_execz .LBB0_765
	v_lshl_add_u32 v0, v30, 2, 0
	s_mov_b64 s[2:3], 0
	v_mov_b32_e32 v2, v30
	s_branch .LBB0_763

; #define LAS __attribute__((address_space(3)))
;     ...
;     unsigned* qhead = (unsigned*)(ws + WS_CTL) + CW_DQ + (qslot * 4 + l) * 64;
;     LAS float* btab = (LAS float*)lds;
;     LAS int* ucur = (LAS int*)(lds + 4 * 132 * 4);
;     LAS unsigned char* KV = lds + 4096;
;     constexpr float LOG2E = 1.4426950408889634f;
;     for (int i = tid; i < 4 * 129; i += NTHR) { const int h = i / 129, n = i % 129; btab[h * 132 + n] = p.in[I_RELB][t5_bucket(n) * 8 + 4 + h] * 5.656854249492381f; }
;     if (tid < 4) { float bx = -1e30f; for (int n = 0; n < 32; ++n) bx = fmaxf(bx, p.in[I_RELB][n * 8 + 4 + tid]); btab[tid * 132 + 129] = bx * 5.656854249492381f; }
;     float s1 = 0.f, s2 = 0.f;
;     for (int i = 0; i < 32; ++i) { s1 += p.in[I_LQ1][l * 32 + i] * p.in[I_LK1][l * 32 + i]; s2 += p.in[I_LQ2][l * 32 + i] * p.in[I_LK2][l * 32 + i]; }
;     const float lam_init = 0.8f - 0.6f * expf(-0.3f * (float)l), lam = expf(s1) - expf(s2) + lam_init;
;     const float c2 = 0.17677669529663687f * LOG2E;
.LBB0_767:
	s_or_b64 exec, exec, s[0:1]
	s_ashr_i32 s21, s20, 6
	s_add_u32 s8, s6, 0x4090000
	s_addc_u32 s9, s7, 0
	s_add_u32 s42, s6, 0x1e674c00
	v_readlane_b32 s22, v254, 49
	s_addc_u32 s43, s7, 0
	s_lshl_b32 s40, s22, 6
	s_lshl_b64 s[10:11], s[40:41], 2
	s_add_u32 s0, s6, s10
	s_addc_u32 s1, s7, s11
	v_readlane_b32 s48, v253, 12
	s_add_u32 s16, s0, 0x4100
	v_readlane_b32 s56, v253, 20
	v_readlane_b32 s57, v253, 21
	s_addc_u32 s17, s1, 0
	s_lshl_b32 s16, s22, 11
	s_lshl_b32 s17, s64, 8
	s_add_i32 s16, s16, s17
	s_add_i32 s16, s16, 0x8000
	s_add_u32 s16, s6, s16
	s_addc_u32 s17, s7, 0
	s_lshl_b32 s40, s22, 5
	v_readlane_b32 s58, v253, 22
	v_readlane_b32 s59, v253, 23
	v_readlane_b32 s60, v253, 24
	v_readlane_b32 s61, v253, 25
	v_readlane_b32 s62, v253, 26
	v_readlane_b32 s63, v253, 27
	s_mov_b64 s[24:25], s[56:57]
	s_lshl_b64 s[4:5], s[40:41], 2
	s_mov_b64 s[30:31], s[62:63]
	v_readlane_b32 s49, v253, 13
	v_readlane_b32 s50, v253, 14
	v_readlane_b32 s51, v253, 15
	v_readlane_b32 s52, v253, 16
	v_readlane_b32 s53, v253, 17
	v_readlane_b32 s54, v253, 18
	v_readlane_b32 s55, v253, 19
	s_add_u32 s18, s30, s4
	s_mov_b64 s[26:27], s[58:59]
	s_mov_b64 s[28:29], s[60:61]
	s_addc_u32 s19, s31, s5
	v_readlane_b32 s48, v253, 30
	v_readlane_b32 s49, v253, 31
	s_add_u32 s2, s48, s4
	v_readlane_b32 s50, v253, 32
	s_addc_u32 s3, s49, s5
	v_readlane_b32 s51, v253, 33
	s_add_u32 s0, s50, s4
	v_readlane_b32 s52, v253, 34
	s_addc_u32 s1, s51, s5
	global_load_dwordx4 v[2:5], v1, s[18:19] offset:48
	global_load_dwordx4 v[6:9], v1, s[18:19] offset:32
	global_load_dwordx4 v[10:13], v1, s[18:19] offset:16
	global_load_dwordx4 v[14:17], v1, s[18:19]
	v_readlane_b32 s53, v253, 35
	global_load_dwordx4 v[18:21], v1, s[2:3] offset:48
	global_load_dwordx4 v[22:25], v1, s[2:3] offset:32
	global_load_dwordx4 v[26:29], v1, s[2:3] offset:16
	global_load_dwordx4 v[34:37], v1, s[2:3]
	s_add_u32 s4, s52, s4
	s_addc_u32 s5, s53, s5
	global_load_dwordx4 v[38:41], v1, s[0:1] offset:48
	global_load_dwordx4 v[42:45], v1, s[0:1] offset:32
	global_load_dwordx4 v[46:49], v1, s[0:1] offset:16
	global_load_dwordx4 v[50:53], v1, s[0:1]
	global_load_dwordx4 v[54:57], v1, s[4:5] offset:48
	global_load_dwordx4 v[58:61], v1, s[4:5] offset:32
	global_load_dwordx4 v[62:65], v1, s[4:5] offset:16
	global_load_dwordx4 v[66:69], v1, s[4:5]
	s_lshl_b32 s46, s21, 5
	s_cmp_lt_u32 s20, 64
	v_and_b32_e32 v31, 63, v32
	v_and_b32_e32 v149, 31, v32
	v_bfe_u32 v0, v32, 5, 1
	v_readlane_b32 s54, v253, 36
	v_readlane_b32 s55, v253, 37
	v_lshlrev_b32_e32 v186, 2, v0
	v_mov_b32_e32 v143, v1
	v_mov_b32_e32 v145, v1
	v_mov_b32_e32 v99, v1
	v_mov_b32_e32 v100, v1
	v_mov_b32_e32 v101, v1
	v_readlane_b32 s56, v253, 38
	v_readlane_b32 s57, v253, 39
	v_readlane_b32 s58, v253, 40
	v_readlane_b32 s59, v253, 41
	v_readlane_b32 s60, v253, 42
	v_readlane_b32 s61, v253, 43
	v_readlane_b32 s62, v253, 44
	v_readlane_b32 s63, v253, 45
	s_waitcnt vmcnt(8)
	v_fma_f32 v34, v14, v34, 0
	v_fmac_f32_e32 v34, v15, v35
	v_fmac_f32_e32 v34, v16, v36
	v_fmac_f32_e32 v34, v17, v37
	s_waitcnt vmcnt(0)
	v_fma_f32 v33, v50, v66, 0
	v_fmac_f32_e32 v33, v51, v67
	v_fmac_f32_e32 v33, v52, v68
	v_fmac_f32_e32 v34, v10, v26
	v_fmac_f32_e32 v33, v53, v69
	v_fmac_f32_e32 v34, v11, v27
	v_fmac_f32_e32 v33, v46, v62
	v_fmac_f32_e32 v34, v12, v28
	v_fmac_f32_e32 v33, v47, v63
	v_fmac_f32_e32 v34, v13, v29
	v_fmac_f32_e32 v33, v48, v64
	v_fmac_f32_e32 v34, v6, v22
	v_fmac_f32_e32 v33, v49, v65
	v_fmac_f32_e32 v34, v7, v23
	v_fmac_f32_e32 v33, v42, v58
	v_fmac_f32_e32 v34, v8, v24
	v_fmac_f32_e32 v33, v43, v59
	v_fmac_f32_e32 v34, v9, v25
	v_fmac_f32_e32 v33, v44, v60
	v_fmac_f32_e32 v34, v2, v18
	v_fmac_f32_e32 v33, v45, v61
	v_fmac_f32_e32 v34, v3, v19
	v_fmac_f32_e32 v33, v38, v54
	v_fmac_f32_e32 v34, v4, v20
	v_fmac_f32_e32 v33, v39, v55
	v_fmac_f32_e32 v34, v5, v21
	global_load_dwordx4 v[2:5], v1, s[18:19] offset:112
	global_load_dwordx4 v[10:13], v1, s[18:19] offset:96
	global_load_dwordx4 v[18:21], v1, s[18:19] offset:80
	global_load_dwordx4 v[26:29], v1, s[18:19] offset:64
	global_load_dwordx4 v[6:9], v1, s[2:3] offset:112
	global_load_dwordx4 v[14:17], v1, s[2:3] offset:96
	global_load_dwordx4 v[22:25], v1, s[2:3] offset:80
	global_load_dwordx4 v[36:39], v1, s[2:3] offset:64
	v_fmac_f32_e32 v33, v40, v56
	v_fmac_f32_e32 v33, v41, v57
	global_load_dwordx4 v[40:43], v1, s[0:1] offset:112
	global_load_dwordx4 v[44:47], v1, s[0:1] offset:96
	global_load_dwordx4 v[48:51], v1, s[0:1] offset:80
	global_load_dwordx4 v[52:55], v1, s[0:1] offset:64
	global_load_dwordx4 v[56:59], v1, s[4:5] offset:112
	global_load_dwordx4 v[60:63], v1, s[4:5] offset:96
	global_load_dwordx4 v[64:67], v1, s[4:5] offset:80
	global_load_dwordx4 v[68:71], v1, s[4:5] offset:64
	s_mov_b32 s0, 0x3fb8aa3b
	s_mov_b32 s1, 0xc2ce8ed0
	s_mov_b32 s2, 0x42b17218
	v_readlane_b32 s4, v255, 14
	v_readlane_b32 s5, v255, 15
	s_cselect_b64 s[18:19], -1, 0
	s_lshl_b64 s[26:27], s[4:5], 2
	s_waitcnt vmcnt(8)
;     ...
;     for (int i = 0; i < 32; ++i) { s1 += p.in[I_LQ1][l * 32 + i] * p.in[I_LK1][l * 32 + i]; s2 += p.in[I_LQ2][l * 32 + i] * p.in[I_LK2][l * 32 + i]; }
;     const float lam_init = 0.8f - 0.6f * expf(-0.3f * (float)l), lam = expf(s1) - expf(s2) + lam_init;
;     const float c2 = 0.17677669529663687f * LOG2E;
;     const int krow = tid >> 3, kch = tid & 7;
;     ...
;         const bf16_t* kbase = U + (size_t)b * LT * INW + C_KD + h * 64;
;         const bf16_t* vbase = VT + (size_t)bh * 64 * LTP;
;         const unsigned koff = (unsigned)(krow * INW + kch * 8), voff = (unsigned)(krow * LTP + kch * 8);
;         const float farraw = btab[h * 132 + 128];
	v_fmac_f32_e32 v34, v26, v36
	v_fmac_f32_e32 v34, v27, v37
	v_fmac_f32_e32 v34, v28, v38
	v_fmac_f32_e32 v34, v29, v39
	v_fmac_f32_e32 v34, v18, v22
	v_fmac_f32_e32 v34, v19, v23
	v_fmac_f32_e32 v34, v20, v24
	v_fmac_f32_e32 v34, v21, v25
	v_fmac_f32_e32 v34, v10, v14
	v_fmac_f32_e32 v34, v11, v15
	v_fmac_f32_e32 v34, v12, v16
	v_fmac_f32_e32 v34, v13, v17
	v_fmac_f32_e32 v34, v2, v6
	v_cvt_f32_u32_e32 v2, s22
	v_fmac_f32_e32 v34, v3, v7
	v_fmac_f32_e32 v34, v4, v8
	v_fmac_f32_e32 v34, v5, v9
	v_mul_f32_e32 v2, 0xbe99999a, v2
	v_mul_f32_e32 v3, 0x3fb8aa3b, v2
	v_fma_f32 v4, v2, s0, -v3
	v_rndne_f32_e32 v5, v3
	v_fmac_f32_e32 v4, 0x32a5705f, v2
	v_sub_f32_e32 v3, v3, v5
	s_waitcnt vmcnt(0)
	v_fmac_f32_e32 v33, v52, v68
	v_add_f32_e32 v3, v3, v4
	v_fmac_f32_e32 v33, v53, v69
	v_exp_f32_e32 v3, v3
	v_cvt_i32_f32_e32 v4, v5
	v_fmac_f32_e32 v33, v54, v70
	v_fmac_f32_e32 v33, v55, v71
	v_fmac_f32_e32 v33, v48, v64
	v_fmac_f32_e32 v33, v49, v65
	v_ldexp_f32 v3, v3, v4
	v_cmp_ngt_f32_e32 vcc, s1, v2
	v_fmac_f32_e32 v33, v50, v66
	v_mov_b32_e32 v7, 0x7f800000
	v_cndmask_b32_e32 v3, 0, v3, vcc
	v_cmp_nlt_f32_e32 vcc, s2, v2
	v_fmac_f32_e32 v33, v51, v67
	v_fmac_f32_e32 v33, v44, v60
	v_cndmask_b32_e32 v2, v7, v3, vcc
	v_mov_b32_e32 v3, 0x3f4ccccd
	v_fmamk_f32 v3, v2, 0xbf19999a, v3
	v_mul_f32_e32 v2, 0x3fb8aa3b, v34
	v_fmac_f32_e32 v33, v45, v61
	v_fma_f32 v4, v34, s0, -v2
	v_rndne_f32_e32 v5, v2
	v_fmac_f32_e32 v33, v46, v62
	v_fmac_f32_e32 v4, 0x32a5705f, v34
	v_sub_f32_e32 v2, v2, v5
	v_fmac_f32_e32 v33, v47, v63
	v_add_f32_e32 v2, v2, v4
	v_fmac_f32_e32 v33, v40, v56
	v_exp_f32_e32 v2, v2
	v_cvt_i32_f32_e32 v4, v5
	v_fmac_f32_e32 v33, v41, v57
	v_fmac_f32_e32 v33, v42, v58
	v_fmac_f32_e32 v33, v43, v59
	v_ldexp_f32 v2, v2, v4
	v_mul_f32_e32 v4, 0x3fb8aa3b, v33
	v_fma_f32 v5, v33, s0, -v4
	v_rndne_f32_e32 v6, v4
	v_fmac_f32_e32 v5, 0x32a5705f, v33
	v_sub_f32_e32 v4, v4, v6
	v_add_f32_e32 v4, v4, v5
	v_exp_f32_e32 v4, v4
	v_cvt_i32_f32_e32 v5, v6
	v_cmp_ngt_f32_e32 vcc, s1, v34
	v_lshl_add_u32 v6, v31, 4, 0
	s_mul_i32 s0, s21, 0x1800
	v_cndmask_b32_e32 v2, 0, v2, vcc
	v_cmp_nlt_f32_e32 vcc, s2, v34
	v_ldexp_f32 v4, v4, v5
	v_and_b32_e32 v5, 7, v32
	v_cndmask_b32_e32 v2, v7, v2, vcc
	v_cmp_ngt_f32_e32 vcc, s1, v33
	s_add_u32 s1, s6, s26
	s_addc_u32 s4, s7, s27
	v_cndmask_b32_e32 v4, 0, v4, vcc
	v_cmp_nlt_f32_e32 vcc, s2, v33
	s_add_u32 s47, s1, 0x5000
	s_movk_i32 s1, 0xb00
	v_cndmask_b32_e32 v4, v7, v4, vcc
	v_sub_f32_e32 v2, v2, v4
	v_ashrrev_i32_e32 v4, 3, v30
	v_mul_lo_u32 v7, v4, s1
	v_lshlrev_b32_e32 v8, 3, v5
	s_movk_i32 s1, 0x1040
	s_addc_u32 s48, s4, 0
	v_or_b32_e32 v142, v7, v8
	v_mul_lo_u32 v7, v4, s1
	v_mul_lo_u32 v4, v4, s83
	v_lshlrev_b32_e32 v5, 4, v5
	v_add_f32_e32 v184, v3, v2
	v_lshlrev_b32_e32 v2, 3, v0
	v_cmp_gt_u32_e64 s[4:5], 32, v31
	v_add3_u32 v185, 0, v4, v5
	v_lshlrev_b32_e32 v0, 4, v0
	v_mul_u32_u24_e32 v4, 0x90, v149
	v_mov_b32_e32 v5, 0x3f80
	s_add_u32 s20, s54, s10
	v_cmp_eq_u32_e64 s[2:3], 0, v30
	v_or_b32_e32 v144, v7, v8
	v_cndmask_b32_e64 v98, 0, v5, s[4:5]
	v_sub_f32_e32 v187, 1.0, v3
	s_addc_u32 s21, s55, s11
	v_add3_u32 v188, 0, v0, v4
	v_lshlrev_b32_e32 v146, 1, v2
	v_add_u32_e32 v189, s0, v6
	s_branch .LBB0_770

; #define LAS __attribute__((address_space(3)))
; __device__ __forceinline__ float bflo(unsigned w) { return __uint_as_float(w << 16); }
; __device__ __forceinline__ float bfhi(unsigned w) { return __uint_as_float(w & 0xFFFF0000u); }
; __device__ __forceinline__ unsigned pkbf(float lo, float hi) { f32x2_t v = {lo, hi}; bf16x2_t b = __builtin_convertvector(v, bf16x2_t); return __builtin_bit_cast(unsigned, b); }
;     ...
;         const int u = *ucur;
;         if (u >= 17 * 32) break;
;         const int qi = 16 - u / 32, bh = u % 32, b = bh >> 2, h = bh & 3;
;         const int q0 = qi == 0 ? 0 : 16 + 256 * (qi - 1), nkt = qi == 0 ? 1 : 4 * qi + 1;
;         const int q0w = q0 + 32 * wave, qpos = q0w + l31;
;         const bool wave_on = (qi > 0) || (wave == 0);
;         const size_t qrow = (size_t)b * LT + (qpos < LT ? qpos : LT - 1);
;         LAS bf16x8* Qs = (LAS bf16x8*)(lds + 4096 + 4 * DF_KB) + wave * 384 + lane;
;         const float farb = btab[h * 132 + 128] * c2;
;         float mref[2];
;         { const unsigned* kmx = (const unsigned*)(ws + WS_CTL) + CW_KMX + l * 256 + b * 8 + h * 2;
; #pragma unroll
;           for (int c = 0; c < 2; ++c) { float qn2 = 0.f;
; #pragma unroll
;               for (int s = 0; s < 2; ++s) { const u32x4 qv = *(const u32x4*)(U + qrow * INW + C_QD + h * 64 + c * 32 + s * 16 + hi * 8);
;                   const unsigned qw[4] = {qv.x, qv.y, qv.z, qv.w};
;                   { u32x4 qs; qs.x = pkbf(bflo(qw[0]) * c2, bfhi(qw[0]) * c2); qs.y = pkbf(bflo(qw[1]) * c2, bfhi(qw[1]) * c2); qs.z = pkbf(bflo(qw[2]) * c2, bfhi(qw[2]) * c2); qs.w = pkbf(bflo(qw[3]) * c2, bfhi(qw[3]) * c2);
;                     Qs[(c * 2 + s) * 64] = __builtin_bit_cast(bf16x8, qs); }
; #pragma unroll
;                   for (int e = 0; e < 4; ++e) qn2 += bflo(qw[e]) * bflo(qw[e]) + bfhi(qw[e]) * bfhi(qw[e]); }
;               qn2 += __shfl_xor(qn2, 32);
;               const float km2 = __uint_as_float(__hip_atomic_load(kmx + c, __ATOMIC_RELAXED, __HIP_MEMORY_SCOPE_AGENT));
;               mref[c] = (sqrtf(qn2 * km2) * 1.001f + btab[h * 132 + 129]) * c2;
;               { u32x4 qx; qx.x = hi ? 0u : (pkbf(farb - mref[c], 0.f) & 0xffffu); qx.y = 0u; qx.z = 0u; qx.w = 0u; Qs[(4 + c) * 64] = __builtin_bit_cast(bf16x8, qx); } } }
.LBB0_774:
	s_or_b64 exec, exec, s[0:1]
	s_waitcnt lgkmcnt(0)
	s_barrier
	ds_read_b32 v0, v1 offset:2112
	s_movk_i32 s0, 67
	s_waitcnt lgkmcnt(0)
	v_cmp_lt_i32_e32 vcc, s0, v0
	v_readfirstlane_b32 s30, v0
	s_mov_b64 s[0:1], -1
	s_cbranch_vccnz .LBB0_769
	s_lshr_b32 s0, s30, 2
	s_lshl_b32 s0, s0, 5
	s_and_b32 s30, s30, 3
	s_lshl_b32 s30, s30, 3
	s_add_i32 s30, s30, s0
	s_add_i32 s30, s30, s64
	s_ashr_i32 s0, s30, 31
	s_lshr_b32 s0, s0, 27
	s_add_i32 s0, s30, s0
	s_ashr_i32 s35, s0, 5
	s_andn2_b32 s0, s0, 31
	s_sub_i32 s34, s30, s0
	s_lshl_b32 s1, s35, 8
	s_sub_i32 s31, 16, s35
	s_ashr_i32 s0, s34, 2
	s_and_b32 s36, s34, 3
	s_sub_i32 s1, 0xf10, s1
	s_cmp_lg_u32 s31, 0
	s_cselect_b32 s49, s1, 0
	s_add_i32 s49, s49, s46
	s_mul_i32 s22, s0, 0x1010
	s_mul_i32 s1, s36, 0x210
	s_lshl_b32 s0, s0, 3
	v_add_u32_e32 v148, s49, v149
	s_add_i32 s50, s1, 0
	s_ashr_i32 s1, s0, 31
	s_ashr_i32 s23, s22, 31
	v_min_i32_e32 v2, 0x100f, v148
	s_lshl_b64 s[0:1], s[0:1], 2
	v_ashrrev_i32_e32 v3, 31, v2
	s_add_u32 s0, s47, s0
	v_lshl_add_u64 v[2:3], v[2:3], 0, s[22:23]
	s_addc_u32 s1, s48, s1
	s_lshl_b32 s28, s36, 3
	v_mov_b64_e32 v[4:5], s[8:9]
	s_add_u32 s24, s0, s28
	v_mad_u64_u32 v[4:5], s[38:39], v2, s97, v[4:5]
	s_addc_u32 s25, s1, 0
	v_mad_i32_i24 v5, v3, s97, v5
	s_lshl_b32 s40, s36, 7
	v_lshl_add_u64 v[2:3], v[4:5], 0, s[40:41]
	v_mov_b32_e32 v147, v1
	v_lshl_add_u64 v[4:5], v[2:3], 0, v[146:147]
	global_load_dwordx4 v[6:9], v[4:5], off offset:1024
	v_mov_b32_e32 v0, s50
	ds_read_b32 v0, v0 offset:512
	v_and_b32_e32 v2, 64, v222
	v_add_u32_e32 v2, 64, v2
	s_waitcnt lgkmcnt(0)
	v_mul_f32_e32 v12, 0x3e8293ee, v0
	v_xor_b32_e32 v0, 32, v222
	v_cmp_lt_i32_e32 vcc, v0, v2
	s_waitcnt vmcnt(0)
	v_lshlrev_b32_e32 v2, 16, v6
	v_and_b32_e32 v3, 0xffff0000, v6
	v_pk_mul_f32 v[10:11], v[2:3], s[92:93] op_sel_hi:[1,0]
	v_pk_mul_f32 v[2:3], v[2:3], v[2:3]
	v_cvt_pk_bf16_f32 v6, v10, v11
	v_lshlrev_b32_e32 v10, 16, v7
	v_and_b32_e32 v11, 0xffff0000, v7
	v_pk_mul_f32 v[14:15], v[10:11], s[92:93] op_sel_hi:[1,0]
	v_add_f32_e32 v2, v2, v3
	v_cvt_pk_bf16_f32 v7, v14, v15
	v_lshlrev_b32_e32 v14, 16, v8
	v_and_b32_e32 v15, 0xffff0000, v8
	v_pk_mul_f32 v[16:17], v[14:15], s[92:93] op_sel_hi:[1,0]
	v_cndmask_b32_e32 v0, v222, v0, vcc
	v_cvt_pk_bf16_f32 v8, v16, v17
	v_lshlrev_b32_e32 v16, 16, v9
	v_and_b32_e32 v17, 0xffff0000, v9
	v_pk_mul_f32 v[18:19], v[16:17], s[92:93] op_sel_hi:[1,0]
	v_lshlrev_b32_e32 v190, 2, v0
	v_cvt_pk_bf16_f32 v9, v18, v19
	ds_write_b128 v189, v[6:9] offset:40960
	v_pk_mul_f32 v[8:9], v[10:11], v[10:11]
	v_pk_mul_f32 v[6:7], v[14:15], v[14:15]
	v_pk_mul_f32 v[10:11], v[16:17], v[16:17]
	global_load_dwordx4 v[14:17], v[4:5], off offset:1056
	v_add_f32_e32 v8, v8, v9
	v_add_f32_e32 v2, v2, v8
	v_add_f32_e32 v3, v6, v7
	v_add_f32_e32 v0, v10, v11
	v_add_f32_e32 v2, v3, v2
	v_add_f32_e32 v0, v0, v2
	s_waitcnt vmcnt(0)
	v_lshlrev_b32_e32 v18, 16, v14
	v_and_b32_e32 v19, 0xffff0000, v14
	v_pk_mul_f32 v[20:21], v[18:19], s[92:93] op_sel_hi:[1,0]
	s_nop 0
	v_cvt_pk_bf16_f32 v14, v20, v21
	v_lshlrev_b32_e32 v20, 16, v15
	v_and_b32_e32 v21, 0xffff0000, v15
	v_pk_mul_f32 v[22:23], v[20:21], s[92:93] op_sel_hi:[1,0]
	s_nop 0
	v_cvt_pk_bf16_f32 v15, v22, v23
	v_lshlrev_b32_e32 v22, 16, v16
	v_and_b32_e32 v23, 0xffff0000, v16
	v_pk_mul_f32 v[24:25], v[22:23], s[92:93] op_sel_hi:[1,0]
	s_nop 0
	v_cvt_pk_bf16_f32 v16, v24, v25
	v_lshlrev_b32_e32 v24, 16, v17
	v_and_b32_e32 v25, 0xffff0000, v17
	v_pk_mul_f32 v[26:27], v[24:25], s[92:93] op_sel_hi:[1,0]
	s_nop 0
	v_cvt_pk_bf16_f32 v17, v26, v27
	ds_write_b128 v189, v[14:17] offset:41984
	v_pk_mul_f32 v[14:15], v[18:19], v[18:19]
	v_pk_mul_f32 v[16:17], v[20:21], v[20:21]
	v_add_f32_e32 v2, v14, v15
	v_pk_mul_f32 v[18:19], v[22:23], v[22:23]
	v_add_f32_e32 v0, v2, v0
	v_add_f32_e32 v2, v16, v17
	v_pk_mul_f32 v[20:21], v[24:25], v[24:25]
	v_add_f32_e32 v0, v2, v0
	v_add_f32_e32 v2, v18, v19
	v_add_f32_e32 v0, v2, v0
	v_add_f32_e32 v2, v20, v21
	v_add_f32_e32 v2, v2, v0
	v_mov_b32_e32 v0, s28
	global_load_dword v6, v0, s[0:1] sc1
	ds_bpermute_b32 v3, v190, v2
	v_mov_b32_e32 v18, 0
	v_mov_b32_e32 v0, 0
	s_and_saveexec_b64 s[28:29], s[4:5]
	s_cbranch_execz .LBB0_777
	s_waitcnt lgkmcnt(0)
	v_add_f32_e32 v0, v2, v3
	s_waitcnt vmcnt(0)
	v_mul_f32_e32 v0, v0, v6
	s_mov_b32 s0, 0xf800000
	v_mul_f32_e32 v2, 0x4f800000, v0
	v_cmp_gt_f32_e32 vcc, s0, v0
	s_nop 1
	v_cndmask_b32_e32 v0, v0, v2, vcc
	v_sqrt_f32_e32 v2, v0
	s_nop 0
	v_add_u32_e32 v3, -1, v2
	v_fma_f32 v7, -v3, v2, v0
	v_add_u32_e32 v6, 1, v2
	v_cmp_ge_f32_e64 s[0:1], 0, v7
	s_nop 1
	v_cndmask_b32_e64 v3, v2, v3, s[0:1]
	v_fma_f32 v2, -v6, v2, v0
	v_cmp_lt_f32_e64 s[0:1], 0, v2
	s_nop 1
	v_cndmask_b32_e64 v2, v3, v6, s[0:1]
	v_mov_b32_e32 v3, s50
	ds_read_b32 v3, v3 offset:516
	v_mul_f32_e32 v6, 0x37800000, v2
	v_cndmask_b32_e32 v2, v2, v6, vcc
	v_cmp_class_f32_e32 vcc, v0, v250
	s_nop 1
	v_cndmask_b32_e32 v0, v2, v0, vcc
	s_waitcnt lgkmcnt(0)
	v_fmac_f32_e32 v3, 0x3f8020c5, v0
	v_fmamk_f32 v0, v3, 0xbe8293ee, v12
	v_cvt_pk_bf16_f32 v0, v0, 0
	v_and_b32_e32 v0, 0xffff, v0
